# scan staging waves prefetch their global operands two chunks ahead (loads issued at the end of the previous iteration, flying across the chunk barrier)
# baseline (speedup 1.0000x reference)
; __device__ __forceinline__ void scan_head(const Params& p, LAS unsigned char* lds, int bh, const int wave) {
;     ...
;         } else {
;             if (chunk + 1 < NCH) SCAN_ISSUE(chunk + 1);
;             if (chunk > 0) SCAN_POST(chunk - 1);
;             if (chunk + 1 < NCH) SCAN_STAGE(chunk + 1);
;         }
;         __syncthreads();
;     }
;     if (wave >= 4) SCAN_POST(NCH - 1);
.Lmy_pf_last:
	s_waitcnt vmcnt(0)
	s_branch .LBB0_805
.LBB0_789:
	s_mov_b32 s51, s2

; __device__ __forceinline__ void scan_head(const Params& p, LAS unsigned char* lds, int bh, const int wave) {
;     ...
;             if (chunk + 1 < NCH) SCAN_ISSUE(chunk + 1);
.LBB0_791:
	s_mov_b64 s[14:15], -1
	s_and_b64 vcc, exec, s[42:43]
	s_cbranch_vccz .LBB0_806
	s_add_i32 s52, s51, 1
	s_cmp_lg_u32 s51, 63
	s_cselect_b64 s[14:15], -1, 0
	s_cmp_eq_u32 s51, 63
	s_cbranch_scc1 .LBB0_794
	s_cmp_lg_u32 s51, 0
	s_cbranch_scc1 .LBB0_794
	v_lshl_or_b32 v10, s52, 5, v125
	v_mov_b32_e32 v11, v48
	v_lshl_add_u64 v[10:11], s[40:41], 0, v[10:11]
	v_mov_b64_e32 v[12:13], s[58:59]
	v_mad_u64_u32 v[12:13], s[60:61], v10, s35, v[12:13]
	v_mov_b32_e32 v8, v124
	v_mov_b32_e32 v14, v13
	v_mad_u64_u32 v[14:15], s[60:61], v11, s35, v[14:15]
	v_ashrrev_i32_e32 v9, 31, v8
	v_mov_b32_e32 v13, v14
	v_lshlrev_b64 v[14:15], 1, v[8:9]
	v_lshl_add_u64 v[12:13], v[12:13], 0, v[14:15]
	s_movk_i32 s2, 0x1000
	v_add_co_u32_e32 v50, vcc, s2, v12
	s_movk_i32 s2, 0xc000
	s_nop 0
	v_addc_co_u32_e32 v51, vcc, 0, v13, vcc
	v_add_co_u32_e32 v80, vcc, s2, v12
	s_movk_i32 s2, 0xd000
	s_nop 0
	v_addc_co_u32_e32 v81, vcc, -1, v13, vcc
	global_load_dwordx4 v[72:75], v[12:13], off
	global_load_dwordx4 v[68:71], v[12:13], off offset:2048
	v_add_co_u32_e32 v12, vcc, s2, v12
	global_load_dwordx4 v[76:79], v[50:51], off
	s_nop 0
	global_load_dwordx4 v[80:83], v[80:81], off offset:-1024
	v_addc_co_u32_e32 v13, vcc, -1, v13, vcc
	global_load_dwordx4 v[88:91], v[12:13], off offset:-3072
	global_load_dwordx4 v[84:87], v[12:13], off offset:-1024
	v_lshlrev_b64 v[12:13], 11, v[10:11]
	v_lshlrev_b64 v[10:11], 12, v[10:11]
	v_lshl_add_u64 v[50:51], s[66:67], 0, v[12:13]
	v_lshl_add_u64 v[12:13], s[68:69], 0, v[12:13]
	v_lshl_add_u64 v[10:11], s[64:65], 0, v[10:11]
	v_lshl_add_u64 v[50:51], v[50:51], 0, v[14:15]
	v_lshl_add_u64 v[12:13], v[12:13], 0, v[14:15]
	v_lshl_add_u64 v[8:9], v[8:9], 2, v[10:11]
	global_load_dwordx4 v[92:95], v[50:51], off nt
	global_load_dwordx4 v[96:99], v[12:13], off nt
	s_nop 0
	global_load_dwordx4 v[12:15], v[8:9], off offset:16 nt
	s_nop 0
	global_load_dwordx4 v[8:11], v[8:9], off nt

; __device__ __forceinline__ void scan_head(const Params& p, LAS unsigned char* lds, int bh, const int wave) {
;     ...
;         } else {
;             if (chunk + 1 < NCH) SCAN_ISSUE(chunk + 1);
;             if (chunk > 0) SCAN_POST(chunk - 1);
;             if (chunk + 1 < NCH) SCAN_STAGE(chunk + 1);
;         }
;         __syncthreads();
.LBB0_804:
	s_or_b64 exec, exec, s[14:15]
	s_waitcnt vmcnt(0)
	s_cmp_gt_u32 s51, 61
	s_cbranch_scc1 .Lmy_pf_skip
	s_add_i32 s98, s51, 2
	v_lshl_or_b32 v10, s98, 5, v125
	v_mov_b32_e32 v11, v48
	v_lshl_add_u64 v[10:11], s[40:41], 0, v[10:11]
	v_mov_b64_e32 v[12:13], s[58:59]
	v_mad_u64_u32 v[12:13], s[60:61], v10, s35, v[12:13]
	v_mov_b32_e32 v8, v124
	v_mov_b32_e32 v14, v13
	v_mad_u64_u32 v[14:15], s[60:61], v11, s35, v[14:15]
	v_ashrrev_i32_e32 v9, 31, v8
	v_mov_b32_e32 v13, v14
	v_lshlrev_b64 v[14:15], 1, v[8:9]
	v_lshl_add_u64 v[12:13], v[12:13], 0, v[14:15]
	s_movk_i32 s2, 0x1000
	v_add_co_u32_e32 v50, vcc, s2, v12
	s_movk_i32 s2, 0xc000
	s_nop 0
	v_addc_co_u32_e32 v51, vcc, 0, v13, vcc
	v_add_co_u32_e32 v80, vcc, s2, v12
	s_movk_i32 s2, 0xd000
	s_nop 0
	v_addc_co_u32_e32 v81, vcc, -1, v13, vcc
	global_load_dwordx4 v[72:75], v[12:13], off
	global_load_dwordx4 v[68:71], v[12:13], off offset:2048
	v_add_co_u32_e32 v12, vcc, s2, v12
	global_load_dwordx4 v[76:79], v[50:51], off
	s_nop 0
	global_load_dwordx4 v[80:83], v[80:81], off offset:-1024
	v_addc_co_u32_e32 v13, vcc, -1, v13, vcc
	global_load_dwordx4 v[88:91], v[12:13], off offset:-3072
	global_load_dwordx4 v[84:87], v[12:13], off offset:-1024
	v_lshlrev_b64 v[12:13], 11, v[10:11]
	v_lshlrev_b64 v[10:11], 12, v[10:11]
	v_lshl_add_u64 v[50:51], s[66:67], 0, v[12:13]
	v_lshl_add_u64 v[12:13], s[68:69], 0, v[12:13]
	v_lshl_add_u64 v[10:11], s[64:65], 0, v[10:11]
	v_lshl_add_u64 v[50:51], v[50:51], 0, v[14:15]
	v_lshl_add_u64 v[12:13], v[12:13], 0, v[14:15]
	v_lshl_add_u64 v[8:9], v[8:9], 2, v[10:11]
	global_load_dwordx4 v[92:95], v[50:51], off nt
	global_load_dwordx4 v[96:99], v[12:13], off nt
	s_nop 0
	global_load_dwordx4 v[12:15], v[8:9], off offset:16 nt
	s_nop 0
	global_load_dwordx4 v[8:11], v[8:9], off nt
.Lmy_pf_skip:
	s_mov_b32 s2, s52
